# diff-attn pair loop: K-fragment ds_reads hoisted above LDS-DMA issue and double-buffered, DMA issues spread between QK MFMA groups, PV MFMA pairs split
# speedup vs baseline: 1.0238x; 1.0238x over previous
.LBB0_374:
	s_mul_hi_u32 s6, s36, 0xaaaaaaab
	s_lshr_b32 s6, s6, 1
	s_mul_i32 s6, s6, 0xffff4000
	s_add_i32 s51, s23, s6
	s_mul_i32 s6, s37, 0xab
	s_bfe_u32 s6, s6, 0x70009
	s_mul_i32 s6, s6, 3
	s_sub_i32 s6, s37, s6
	s_and_b32 s6, s6, 0xff
	s_add_i32 s46, s37, -1
	s_lshl_b32 s6, s6, 14
	s_cmp_lg_u32 0, -1
	s_cselect_b32 s7, 0, 0
	s_add_i32 s6, s7, s6
	s_add_i32 s53, s6, 0x10000
	s_waitcnt vmcnt(0)
	s_barrier
	ds_read_b128 v[132:135], v181 offset:32768
	ds_read_b128 v[136:139], v181 offset:36864
	ds_read_b128 v[140:143], v182 offset:32768
	ds_read_b128 v[144:147], v182 offset:36864
	ds_read_b128 v[188:191], v181 offset:40960
	ds_read_b128 v[192:195], v181 offset:45056
	ds_read_b128 v[222:225], v182 offset:40960
	ds_read_b128 v[226:229], v182 offset:45056
	s_add_i32 s47, s50, 0x8000
	s_add_i32 m0, s53, s22
	s_mov_b32 s6, s42
	buffer_load_dwordx4 v183, s[40:43], s47 offen lds
	s_mov_b32 s7, s43
	s_mov_b32 m0, s23
	s_add_i32 s54, s44, 0xc0000
	buffer_load_dwordx4 v184, s[4:7], s44 offen lds
	s_waitcnt lgkmcnt(6)
	v_mfma_f32_16x16x32_bf16 v[28:31], v[132:135], v[120:123], v[36:39]
	v_mfma_f32_16x16x32_bf16 v[230:233], v[132:135], v[124:127], v[36:39]
	v_mfma_f32_16x16x32_bf16 v[234:237], v[136:139], v[120:123], v[36:39]
	v_mfma_f32_16x16x32_bf16 v[238:241], v[136:139], v[124:127], v[36:39]
	s_waitcnt lgkmcnt(4)
	v_mfma_f32_16x16x32_bf16 v[28:31], v[140:143], v[116:119], v[28:31]
	v_mfma_f32_16x16x32_bf16 v[230:233], v[140:143], v[128:131], v[230:233]
	v_mfma_f32_16x16x32_bf16 v[234:237], v[144:147], v[116:119], v[234:237]
	v_mfma_f32_16x16x32_bf16 v[238:241], v[144:147], v[128:131], v[238:241]
	ds_read_b128 v[132:135], v181 offset:49152
	ds_read_b128 v[136:139], v181 offset:53248
	ds_read_b128 v[140:143], v182 offset:49152
	ds_read_b128 v[144:147], v182 offset:53248
	s_mov_b32 m0, s24
	s_nop 0
	buffer_load_dwordx4 v184, s[4:7], s54 offen lds
	s_waitcnt lgkmcnt(6)
	v_mfma_f32_16x16x32_bf16 v[168:171], v[188:191], v[120:123], v[36:39]
	v_mfma_f32_16x16x32_bf16 v[164:167], v[188:191], v[124:127], v[36:39]
	v_mfma_f32_16x16x32_bf16 v[160:163], v[192:195], v[120:123], v[36:39]
	v_mfma_f32_16x16x32_bf16 v[156:159], v[192:195], v[124:127], v[36:39]
	s_waitcnt lgkmcnt(4)
	v_mfma_f32_16x16x32_bf16 v[168:171], v[222:225], v[116:119], v[168:171]
	v_mfma_f32_16x16x32_bf16 v[164:167], v[222:225], v[128:131], v[164:167]
	v_mfma_f32_16x16x32_bf16 v[160:163], v[226:229], v[116:119], v[160:163]
	v_mfma_f32_16x16x32_bf16 v[156:159], v[226:229], v[128:131], v[156:159]
	ds_read_b128 v[188:191], v181 offset:57344
	ds_read_b128 v[192:195], v181 offset:61440
	ds_read_b128 v[222:225], v182 offset:57344
	ds_read_b128 v[226:229], v182 offset:61440
	s_add_i32 m0, s53, s25
	s_nop 0
	buffer_load_dwordx4 v185, s[40:43], s47 offen lds
	s_waitcnt lgkmcnt(6)
	v_mfma_f32_16x16x32_bf16 v[24:27], v[132:135], v[120:123], v[36:39]
	v_mfma_f32_16x16x32_bf16 v[32:35], v[132:135], v[124:127], v[36:39]
	v_mfma_f32_16x16x32_bf16 v[152:155], v[136:139], v[120:123], v[36:39]
	v_mfma_f32_16x16x32_bf16 v[148:151], v[136:139], v[124:127], v[36:39]
	s_waitcnt lgkmcnt(4)
	v_mfma_f32_16x16x32_bf16 v[24:27], v[140:143], v[116:119], v[24:27]
	v_mfma_f32_16x16x32_bf16 v[32:35], v[140:143], v[128:131], v[32:35]
	v_mfma_f32_16x16x32_bf16 v[152:155], v[144:147], v[116:119], v[152:155]
	v_mfma_f32_16x16x32_bf16 v[148:151], v[144:147], v[128:131], v[148:151]
	s_mov_b32 m0, s26
	s_nop 0
	buffer_load_dwordx4 v186, s[4:7], s44 offen lds
	s_waitcnt lgkmcnt(2)
	v_mfma_f32_16x16x32_bf16 v[144:147], v[188:191], v[120:123], v[36:39]
	v_mfma_f32_16x16x32_bf16 v[140:143], v[188:191], v[124:127], v[36:39]
	v_mfma_f32_16x16x32_bf16 v[136:139], v[192:195], v[120:123], v[36:39]
	v_mfma_f32_16x16x32_bf16 v[132:135], v[192:195], v[124:127], v[36:39]
	s_mov_b32 m0, s27
	s_nop 0
	buffer_load_dwordx4 v186, s[4:7], s54 offen lds
	s_waitcnt lgkmcnt(0)
	v_mfma_f32_16x16x32_bf16 v[144:147], v[222:225], v[116:119], v[144:147]
	v_mfma_f32_16x16x32_bf16 v[140:143], v[222:225], v[128:131], v[140:143]
	v_mfma_f32_16x16x32_bf16 v[136:139], v[226:229], v[116:119], v[136:139]
	v_mfma_f32_16x16x32_bf16 v[132:135], v[226:229], v[128:131], v[132:135]
	s_add_i32 s53, s37, 0xfffe
	s_and_b32 s54, s53, 0xff
	s_mulk_i32 s54, 0xab
	s_bfe_u32 s54, s54, 0x70009
	s_mul_i32 s54, s54, 3
	s_sub_i32 s53, s53, s54
	s_and_b32 s53, s53, 0xff
	v_lshl_add_u32 v20, s53, 14, v180
	v_add_u32_e32 v20, 0x10000, v20
	v_add_u32_e32 v187, v20, v178
	v_add_u32_e32 v206, v20, v179
	v_exp_f32_e32 v20, v28
	v_exp_f32_e32 v21, v29
	v_exp_f32_e32 v22, v30
	v_exp_f32_e32 v23, v31
	v_exp_f32_e32 v28, v230
	v_cvt_pk_fp8_f32 v20, v20, v21
	v_exp_f32_e32 v21, v231
	ds_read_b128 v[188:191], v187
	ds_read_b128 v[192:195], v206
	v_mfma_f32_16x16x128_f8f6f4 v[112:115], v[4:11], v[40:43], v[112:115] blgp:4
	ds_read_b128 v[222:225], v187 offset:2048
	ds_read_b128 v[226:229], v206 offset:2048
	v_cvt_pk_fp8_f32 v20, v22, v23 op_sel:[0,0,1]
	v_exp_f32_e32 v22, v232
	v_mfma_f32_16x16x128_f8f6f4 v[88:91], v[12:19], v[40:43], v[88:91] blgp:4
	v_exp_f32_e32 v23, v233
	v_cvt_pk_fp8_f32 v28, v28, v21
	s_waitcnt lgkmcnt(2)
	v_mfma_f32_16x16x128_f8f6f4 v[108:111], v[4:11], v[188:195], v[108:111]
	v_cvt_pk_fp8_f32 v28, v22, v23 op_sel:[0,0,1]
	v_exp_f32_e32 v21, v234
	v_exp_f32_e32 v22, v235
	v_exp_f32_e32 v29, v238
	v_mfma_f32_16x16x128_f8f6f4 v[80:83], v[12:19], v[188:195], v[80:83]
	v_exp_f32_e32 v31, v239
	ds_read_b128 v[188:191], v187 offset:4096
	ds_read_b128 v[192:195], v206 offset:4096
	v_exp_f32_e32 v23, v236
	v_exp_f32_e32 v30, v237
	v_cvt_pk_fp8_f32 v21, v21, v22
	v_exp_f32_e32 v22, v240
	v_exp_f32_e32 v207, v241
	v_cvt_pk_fp8_f32 v29, v29, v31
	v_cvt_pk_fp8_f32 v21, v23, v30 op_sel:[0,0,1]
	s_waitcnt lgkmcnt(2)
	v_mfma_f32_16x16x128_f8f6f4 v[104:107], v[4:11], v[222:229], v[104:107]
	v_cvt_pk_fp8_f32 v29, v22, v207 op_sel:[0,0,1]
	v_exp_f32_e32 v22, v168
	v_exp_f32_e32 v23, v169
	v_exp_f32_e32 v30, v164
	v_mfma_f32_16x16x128_f8f6f4 v[72:75], v[12:19], v[222:229], v[72:75]
	v_exp_f32_e32 v164, v165
	v_exp_f32_e32 v31, v170
	v_exp_f32_e32 v207, v171
	v_cvt_pk_fp8_f32 v22, v22, v23
	v_exp_f32_e32 v23, v166
	v_exp_f32_e32 v211, v167
	v_cvt_pk_fp8_f32 v30, v30, v164
	ds_read_b128 v[164:167], v187 offset:6144
	ds_read_b128 v[168:171], v206 offset:6144
	v_cvt_pk_fp8_f32 v22, v31, v207 op_sel:[0,0,1]
	s_waitcnt lgkmcnt(2)
	v_mfma_f32_16x16x128_f8f6f4 v[100:103], v[4:11], v[188:195], v[100:103]
	v_cvt_pk_fp8_f32 v30, v23, v211 op_sel:[0,0,1]
	v_exp_f32_e32 v23, v160
	v_exp_f32_e32 v160, v161
	v_exp_f32_e32 v31, v156
	v_mfma_f32_16x16x128_f8f6f4 v[64:67], v[12:19], v[188:195], v[64:67]
	v_exp_f32_e32 v156, v157
	v_exp_f32_e32 v188, v162
	v_exp_f32_e32 v189, v163
	v_cvt_pk_fp8_f32 v23, v23, v160
	v_exp_f32_e32 v190, v158
	v_exp_f32_e32 v191, v159
	v_cvt_pk_fp8_f32 v31, v31, v156
	ds_read_b128 v[156:159], v187 offset:8192
	ds_read_b128 v[160:163], v206 offset:8192
	v_cvt_pk_fp8_f32 v23, v188, v189 op_sel:[0,0,1]
	s_waitcnt lgkmcnt(2)
	v_mfma_f32_16x16x128_f8f6f4 v[96:99], v[4:11], v[164:171], v[96:99]
	v_cvt_pk_fp8_f32 v31, v190, v191 op_sel:[0,0,1]
	v_exp_f32_e32 v24, v24
	v_exp_f32_e32 v25, v25
	v_exp_f32_e32 v32, v32
	v_mfma_f32_16x16x128_f8f6f4 v[60:63], v[12:19], v[164:171], v[60:63]
	v_exp_f32_e32 v33, v33
	ds_read_b128 v[164:167], v187 offset:10240
	ds_read_b128 v[168:171], v206 offset:10240
	v_exp_f32_e32 v26, v26
	v_exp_f32_e32 v27, v27
	v_cvt_pk_fp8_f32 v24, v24, v25
	v_exp_f32_e32 v25, v34
	v_exp_f32_e32 v34, v35
	v_cvt_pk_fp8_f32 v32, v32, v33
	v_cvt_pk_fp8_f32 v24, v26, v27 op_sel:[0,0,1]
	s_waitcnt lgkmcnt(2)
	v_mfma_f32_16x16x128_f8f6f4 v[92:95], v[4:11], v[156:163], v[92:95]
	v_cvt_pk_fp8_f32 v32, v25, v34 op_sel:[0,0,1]
	v_exp_f32_e32 v25, v152
	v_exp_f32_e32 v26, v153
	v_exp_f32_e32 v33, v148
	v_mfma_f32_16x16x128_f8f6f4 v[56:59], v[12:19], v[156:163], v[56:59]
	v_exp_f32_e32 v35, v149
	v_exp_f32_e32 v27, v154
	v_exp_f32_e32 v34, v155
	v_cvt_pk_fp8_f32 v25, v25, v26
	v_exp_f32_e32 v26, v150
	v_exp_f32_e32 v156, v151
	ds_read_b128 v[148:151], v187 offset:12288
	ds_read_b128 v[152:155], v206 offset:12288
	v_cvt_pk_fp8_f32 v33, v33, v35
	v_cvt_pk_fp8_f32 v25, v27, v34 op_sel:[0,0,1]
	s_waitcnt lgkmcnt(2)
	v_mfma_f32_16x16x128_f8f6f4 v[84:87], v[4:11], v[164:171], v[84:87]
	v_cvt_pk_fp8_f32 v33, v26, v156 op_sel:[0,0,1]
	v_exp_f32_e32 v26, v144
	v_exp_f32_e32 v27, v145
	v_exp_f32_e32 v34, v140
	v_mfma_f32_16x16x128_f8f6f4 v[52:55], v[12:19], v[164:171], v[52:55]
	v_exp_f32_e32 v140, v141
	v_exp_f32_e32 v35, v146
	v_exp_f32_e32 v156, v147
	v_cvt_pk_fp8_f32 v26, v26, v27
	v_exp_f32_e32 v27, v142
	v_exp_f32_e32 v157, v143
	v_cvt_pk_fp8_f32 v34, v34, v140
	ds_read_b128 v[140:143], v187 offset:14336
	ds_read_b128 v[144:147], v206 offset:14336
	v_cvt_pk_fp8_f32 v26, v35, v156 op_sel:[0,0,1]
	s_waitcnt lgkmcnt(2)
	v_mfma_f32_16x16x128_f8f6f4 v[76:79], v[4:11], v[148:155], v[76:79]
	v_cvt_pk_fp8_f32 v34, v27, v157 op_sel:[0,0,1]
	v_mfma_f32_16x16x128_f8f6f4 v[48:51], v[12:19], v[148:155], v[48:51]
	s_waitcnt lgkmcnt(0)
	v_mfma_f32_16x16x128_f8f6f4 v[68:71], v[4:11], v[140:147], v[68:71]
	v_exp_f32_e32 v27, v136
	v_exp_f32_e32 v4, v137
	v_exp_f32_e32 v5, v138
	v_exp_f32_e32 v6, v139
	v_exp_f32_e32 v35, v132
	v_cvt_pk_fp8_f32 v27, v27, v4
	v_exp_f32_e32 v4, v133
	v_mfma_f32_16x16x128_f8f6f4 v[44:47], v[12:19], v[140:147], v[44:47]
	v_cvt_pk_fp8_f32 v27, v5, v6 op_sel:[0,0,1]
	v_exp_f32_e32 v5, v134
	v_exp_f32_e32 v6, v135
	v_cvt_pk_fp8_f32 v35, v35, v4
	v_cvt_pk_fp8_f32 v35, v5, v6 op_sel:[0,0,1]
	s_add_i32 s53, s50, 0xc000
	s_add_i32 s50, s51, s50
	s_waitcnt vmcnt(0)
	s_barrier
	ds_read_b128 v[132:135], v181
	ds_read_b128 v[136:139], v181 offset:4096
	ds_read_b128 v[140:143], v182
	ds_read_b128 v[144:147], v182 offset:4096
	ds_read_b128 v[164:167], v181 offset:8192
	ds_read_b128 v[168:171], v181 offset:12288
	ds_read_b128 v[188:191], v182 offset:8192
	ds_read_b128 v[192:195], v182 offset:12288
	s_add_i32 m0, s50, 0x1c000
	s_add_i32 s54, s44, 0x180000
	buffer_load_dwordx4 v183, s[40:43], s53 offen lds
	s_mov_b32 m0, s29
	s_add_i32 s55, s44, 0x240000
	buffer_load_dwordx4 v184, s[4:7], s54 offen lds
	s_waitcnt lgkmcnt(6)
	v_mfma_f32_16x16x32_bf16 v[12:15], v[132:135], v[120:123], v[36:39]
	v_mfma_f32_16x16x32_bf16 v[222:225], v[132:135], v[124:127], v[36:39]
	v_mfma_f32_16x16x32_bf16 v[226:229], v[136:139], v[120:123], v[36:39]
	v_mfma_f32_16x16x32_bf16 v[230:233], v[136:139], v[124:127], v[36:39]
	s_waitcnt lgkmcnt(4)
	v_mfma_f32_16x16x32_bf16 v[12:15], v[140:143], v[116:119], v[12:15]
	v_mfma_f32_16x16x32_bf16 v[222:225], v[140:143], v[128:131], v[222:225]
	v_mfma_f32_16x16x32_bf16 v[226:229], v[144:147], v[116:119], v[226:229]
	v_mfma_f32_16x16x32_bf16 v[230:233], v[144:147], v[128:131], v[230:233]
	ds_read_b128 v[132:135], v181 offset:16384
	ds_read_b128 v[136:139], v181 offset:20480
	ds_read_b128 v[140:143], v182 offset:16384
	ds_read_b128 v[144:147], v182 offset:20480
	s_mov_b32 m0, s31
	s_nop 0
	buffer_load_dwordx4 v184, s[4:7], s55 offen lds
	s_waitcnt lgkmcnt(6)
	v_mfma_f32_16x16x32_bf16 v[234:237], v[164:167], v[120:123], v[36:39]
	v_mfma_f32_16x16x32_bf16 v[238:241], v[164:167], v[124:127], v[36:39]
	v_mfma_f32_16x16x32_bf16 v[160:163], v[168:171], v[120:123], v[36:39]
	v_mfma_f32_16x16x32_bf16 v[156:159], v[168:171], v[124:127], v[36:39]
	s_waitcnt lgkmcnt(4)
	v_mfma_f32_16x16x32_bf16 v[234:237], v[188:191], v[116:119], v[234:237]
	v_mfma_f32_16x16x32_bf16 v[238:241], v[188:191], v[128:131], v[238:241]
	v_mfma_f32_16x16x32_bf16 v[160:163], v[192:195], v[116:119], v[160:163]
	v_mfma_f32_16x16x32_bf16 v[156:159], v[192:195], v[128:131], v[156:159]
	ds_read_b128 v[164:167], v181 offset:24576
	ds_read_b128 v[168:171], v181 offset:28672
	ds_read_b128 v[188:191], v182 offset:24576
	ds_read_b128 v[192:195], v182 offset:28672
	s_add_i32 m0, s50, 0x1c400
	s_nop 0
	buffer_load_dwordx4 v185, s[40:43], s53 offen lds
	s_waitcnt lgkmcnt(6)
	v_mfma_f32_16x16x32_bf16 v[8:11], v[132:135], v[120:123], v[36:39]
	v_mfma_f32_16x16x32_bf16 v[16:19], v[132:135], v[124:127], v[36:39]
	v_mfma_f32_16x16x32_bf16 v[152:155], v[136:139], v[120:123], v[36:39]
	v_mfma_f32_16x16x32_bf16 v[148:151], v[136:139], v[124:127], v[36:39]
	s_waitcnt lgkmcnt(4)
	v_mfma_f32_16x16x32_bf16 v[8:11], v[140:143], v[116:119], v[8:11]
	v_mfma_f32_16x16x32_bf16 v[16:19], v[140:143], v[128:131], v[16:19]
	v_mfma_f32_16x16x32_bf16 v[152:155], v[144:147], v[116:119], v[152:155]
	v_mfma_f32_16x16x32_bf16 v[148:151], v[144:147], v[128:131], v[148:151]
	s_mov_b32 m0, s34
	s_nop 0
	buffer_load_dwordx4 v186, s[4:7], s54 offen lds
	s_waitcnt lgkmcnt(2)
	v_mfma_f32_16x16x32_bf16 v[144:147], v[164:167], v[120:123], v[36:39]
	v_mfma_f32_16x16x32_bf16 v[140:143], v[164:167], v[124:127], v[36:39]
	v_mfma_f32_16x16x32_bf16 v[136:139], v[168:171], v[120:123], v[36:39]
	v_mfma_f32_16x16x32_bf16 v[132:135], v[168:171], v[124:127], v[36:39]
	s_mov_b32 m0, s35
	s_nop 0
	buffer_load_dwordx4 v186, s[4:7], s55 offen lds
	s_waitcnt lgkmcnt(0)
	v_mfma_f32_16x16x32_bf16 v[144:147], v[188:191], v[116:119], v[144:147]
	v_mfma_f32_16x16x32_bf16 v[140:143], v[188:191], v[128:131], v[140:143]
	v_mfma_f32_16x16x32_bf16 v[136:139], v[192:195], v[116:119], v[136:139]
	v_mfma_f32_16x16x32_bf16 v[132:135], v[192:195], v[128:131], v[132:135]
	s_mul_i32 s6, s46, 0xab
	s_bfe_u32 s6, s6, 0x70009
	s_mul_i32 s6, s6, 3
	s_sub_i32 s6, s46, s6
	s_and_b32 s6, s6, 0xff
	s_nop 1
	v_lshl_add_u32 v4, s6, 14, v180
	v_add_u32_e32 v4, 0x10000, v4
	v_add_u32_e32 v187, v4, v178
	v_add_u32_e32 v206, v4, v179
	v_exp_f32_e32 v4, v12
	v_exp_f32_e32 v5, v13
	v_exp_f32_e32 v6, v14
	v_exp_f32_e32 v7, v15
	v_exp_f32_e32 v12, v222
	v_cvt_pk_fp8_f32 v4, v4, v5
	v_exp_f32_e32 v5, v223
	ds_read_b128 v[164:167], v187
	ds_read_b128 v[168:171], v206
	v_mfma_f32_16x16x128_f8f6f4 v[112:115], v[20:27], v[40:43], v[112:115] blgp:4
	v_cvt_pk_fp8_f32 v4, v6, v7 op_sel:[0,0,1]
	v_exp_f32_e32 v6, v224
	v_exp_f32_e32 v7, v225
	v_cvt_pk_fp8_f32 v12, v12, v5
	v_mfma_f32_16x16x128_f8f6f4 v[88:91], v[28:35], v[40:43], v[88:91] blgp:4
	ds_read_b128 v[188:191], v187 offset:2048
	ds_read_b128 v[192:195], v206 offset:2048
	s_waitcnt lgkmcnt(2)
	v_mfma_f32_16x16x128_f8f6f4 v[108:111], v[20:27], v[164:171], v[108:111]
	v_cvt_pk_fp8_f32 v12, v6, v7 op_sel:[0,0,1]
	v_exp_f32_e32 v5, v226
	v_exp_f32_e32 v6, v227
	v_exp_f32_e32 v13, v230
	v_mfma_f32_16x16x128_f8f6f4 v[80:83], v[28:35], v[164:171], v[80:83]
	v_exp_f32_e32 v15, v231
	v_exp_f32_e32 v7, v228
	v_exp_f32_e32 v14, v229
	v_cvt_pk_fp8_f32 v5, v5, v6
	v_exp_f32_e32 v6, v232
	v_exp_f32_e32 v207, v233
	v_cvt_pk_fp8_f32 v13, v13, v15
	ds_read_b128 v[164:167], v187 offset:4096
	ds_read_b128 v[168:171], v206 offset:4096
	v_cvt_pk_fp8_f32 v5, v7, v14 op_sel:[0,0,1]
	s_waitcnt lgkmcnt(2)
	v_mfma_f32_16x16x128_f8f6f4 v[104:107], v[20:27], v[188:195], v[104:107]
	v_cvt_pk_fp8_f32 v13, v6, v207 op_sel:[0,0,1]
	v_exp_f32_e32 v6, v234
	v_exp_f32_e32 v7, v235
	v_exp_f32_e32 v14, v238
	v_mfma_f32_16x16x128_f8f6f4 v[72:75], v[28:35], v[188:195], v[72:75]
	v_exp_f32_e32 v188, v239
	v_exp_f32_e32 v15, v236
	v_exp_f32_e32 v207, v237
	v_cvt_pk_fp8_f32 v6, v6, v7
	v_exp_f32_e32 v7, v240
	v_exp_f32_e32 v211, v241
	v_cvt_pk_fp8_f32 v14, v14, v188
	ds_read_b128 v[188:191], v187 offset:6144
	ds_read_b128 v[192:195], v206 offset:6144
	v_cvt_pk_fp8_f32 v6, v15, v207 op_sel:[0,0,1]
	s_waitcnt lgkmcnt(2)
	v_mfma_f32_16x16x128_f8f6f4 v[100:103], v[20:27], v[164:171], v[100:103]
	v_cvt_pk_fp8_f32 v14, v7, v211 op_sel:[0,0,1]
	v_exp_f32_e32 v7, v160
	v_exp_f32_e32 v160, v161
	v_exp_f32_e32 v15, v156
	v_mfma_f32_16x16x128_f8f6f4 v[64:67], v[28:35], v[164:171], v[64:67]
	v_exp_f32_e32 v156, v157
	v_exp_f32_e32 v164, v162
	v_exp_f32_e32 v165, v163
	v_cvt_pk_fp8_f32 v7, v7, v160
	v_exp_f32_e32 v166, v158
	v_exp_f32_e32 v167, v159
	v_cvt_pk_fp8_f32 v15, v15, v156
	ds_read_b128 v[156:159], v187 offset:8192
	ds_read_b128 v[160:163], v206 offset:8192
	v_cvt_pk_fp8_f32 v7, v164, v165 op_sel:[0,0,1]
	s_waitcnt lgkmcnt(2)
	v_mfma_f32_16x16x128_f8f6f4 v[96:99], v[20:27], v[188:195], v[96:99]
	v_cvt_pk_fp8_f32 v15, v166, v167 op_sel:[0,0,1]
	v_exp_f32_e32 v8, v8
	v_exp_f32_e32 v9, v9
	v_exp_f32_e32 v16, v16
	v_mfma_f32_16x16x128_f8f6f4 v[60:63], v[28:35], v[188:195], v[60:63]
	v_exp_f32_e32 v17, v17
	v_exp_f32_e32 v10, v10
	v_exp_f32_e32 v11, v11
	v_cvt_pk_fp8_f32 v8, v8, v9
	v_exp_f32_e32 v9, v18
	v_exp_f32_e32 v18, v19
	v_cvt_pk_fp8_f32 v16, v16, v17
	ds_read_b128 v[164:167], v187 offset:10240
	ds_read_b128 v[168:171], v206 offset:10240
	v_cvt_pk_fp8_f32 v8, v10, v11 op_sel:[0,0,1]
	s_waitcnt lgkmcnt(2)
	v_mfma_f32_16x16x128_f8f6f4 v[92:95], v[20:27], v[156:163], v[92:95]
	v_cvt_pk_fp8_f32 v16, v9, v18 op_sel:[0,0,1]
	v_exp_f32_e32 v9, v152
	v_exp_f32_e32 v10, v153
	v_exp_f32_e32 v17, v148
	v_mfma_f32_16x16x128_f8f6f4 v[56:59], v[28:35], v[156:163], v[56:59]
	v_exp_f32_e32 v19, v149
	v_exp_f32_e32 v11, v154
	v_exp_f32_e32 v18, v155
	v_cvt_pk_fp8_f32 v9, v9, v10
	v_exp_f32_e32 v10, v150
	v_exp_f32_e32 v156, v151
	v_cvt_pk_fp8_f32 v17, v17, v19
	ds_read_b128 v[148:151], v187 offset:12288
	ds_read_b128 v[152:155], v206 offset:12288
	v_cvt_pk_fp8_f32 v9, v11, v18 op_sel:[0,0,1]
	s_waitcnt lgkmcnt(2)
	v_mfma_f32_16x16x128_f8f6f4 v[84:87], v[20:27], v[164:171], v[84:87]
	v_cvt_pk_fp8_f32 v17, v10, v156 op_sel:[0,0,1]
	v_exp_f32_e32 v10, v144
	v_exp_f32_e32 v11, v145
	v_exp_f32_e32 v18, v140
	v_mfma_f32_16x16x128_f8f6f4 v[52:55], v[28:35], v[164:171], v[52:55]
	v_exp_f32_e32 v140, v141
	v_exp_f32_e32 v19, v146
	v_exp_f32_e32 v156, v147
	v_cvt_pk_fp8_f32 v10, v10, v11
	v_exp_f32_e32 v11, v142
	v_exp_f32_e32 v157, v143
	v_cvt_pk_fp8_f32 v18, v18, v140
	ds_read_b128 v[140:143], v187 offset:14336
	ds_read_b128 v[144:147], v206 offset:14336
	v_cvt_pk_fp8_f32 v10, v19, v156 op_sel:[0,0,1]
	s_waitcnt lgkmcnt(2)
	v_mfma_f32_16x16x128_f8f6f4 v[76:79], v[20:27], v[148:155], v[76:79]
	v_cvt_pk_fp8_f32 v18, v11, v157 op_sel:[0,0,1]
	v_exp_f32_e32 v11, v136
	v_exp_f32_e32 v19, v137
	v_mfma_f32_16x16x128_f8f6f4 v[48:51], v[28:35], v[148:155], v[48:51]
	s_waitcnt lgkmcnt(0)
	v_mfma_f32_16x16x128_f8f6f4 v[68:71], v[20:27], v[140:147], v[68:71]
	v_exp_f32_e32 v20, v138
	v_exp_f32_e32 v21, v139
	v_cvt_pk_fp8_f32 v11, v11, v19
	v_exp_f32_e32 v19, v132
	v_exp_f32_e32 v22, v135
	v_mfma_f32_16x16x128_f8f6f4 v[44:47], v[28:35], v[140:147], v[44:47]
	v_cvt_pk_fp8_f32 v11, v20, v21 op_sel:[0,0,1]
	v_exp_f32_e32 v20, v133
	v_exp_f32_e32 v21, v134
	v_cvt_pk_fp8_f32 v19, v19, v20
	v_cvt_pk_fp8_f32 v19, v21, v22 op_sel:[0,0,1]
	s_add_i32 s44, s44, 0x300000
	s_add_i32 s37, s37, 2
	s_add_i32 s36, s36, 2
	s_cmpk_lt_u32 s46, 0x7d
	s_mov_b32 s50, s47
	s_cbranch_scc1 .LBB0_374
	s_waitcnt vmcnt(0)
	s_barrier
	ds_read_b128 v[20:23], v181 offset:32768
	ds_read_b128 v[24:27], v182 offset:32768
	s_waitcnt lgkmcnt(1)
	v_mfma_f32_16x16x32_bf16 v[28:31], v[20:23], v[120:123], v[36:39]
	v_mfma_f32_16x16x32_bf16 v[20:23], v[20:23], v[124:127], v[36:39]
	s_waitcnt lgkmcnt(0)
	v_mfma_f32_16x16x32_bf16 v[144:147], v[24:27], v[116:119], v[28:31]
	v_mfma_f32_16x16x32_bf16 v[20:23], v[24:27], v[128:131], v[20:23]
	ds_read_b128 v[24:27], v181 offset:36864
	s_nop 2
	ds_read_b128 v[28:31], v182 offset:36864
	s_waitcnt lgkmcnt(1)
	v_mfma_f32_16x16x32_bf16 v[32:35], v[24:27], v[120:123], v[36:39]
	v_mfma_f32_16x16x32_bf16 v[24:27], v[24:27], v[124:127], v[36:39]
	s_waitcnt lgkmcnt(0)
	v_mfma_f32_16x16x32_bf16 v[152:155], v[28:31], v[116:119], v[32:35]
	v_mfma_f32_16x16x32_bf16 v[28:31], v[28:31], v[128:131], v[24:27]
	s_nop 4
	ds_read_b128 v[24:27], v181 offset:40960
	ds_read_b128 v[32:35], v182 offset:40960
	s_waitcnt lgkmcnt(1)
	v_mfma_f32_16x16x32_bf16 v[132:135], v[24:27], v[120:123], v[36:39]
	v_mfma_f32_16x16x32_bf16 v[24:27], v[24:27], v[124:127], v[36:39]
	s_waitcnt lgkmcnt(0)
	v_mfma_f32_16x16x32_bf16 v[148:151], v[32:35], v[116:119], v[132:135]
	v_mfma_f32_16x16x32_bf16 v[24:27], v[32:35], v[128:131], v[24:27]
	ds_read_b128 v[32:35], v181 offset:45056
	s_nop 2
	ds_read_b128 v[132:135], v182 offset:45056
	s_waitcnt lgkmcnt(1)
	v_mfma_f32_16x16x32_bf16 v[136:139], v[32:35], v[120:123], v[36:39]
	v_mfma_f32_16x16x32_bf16 v[32:35], v[32:35], v[124:127], v[36:39]
	s_waitcnt lgkmcnt(0)
	v_mfma_f32_16x16x32_bf16 v[160:163], v[132:135], v[116:119], v[136:139]
	v_mfma_f32_16x16x32_bf16 v[132:135], v[132:135], v[128:131], v[32:35]
	s_nop 4
	ds_read_b128 v[32:35], v181 offset:49152
	ds_read_b128 v[136:139], v182 offset:49152
	s_waitcnt lgkmcnt(1)
	v_mfma_f32_16x16x32_bf16 v[140:143], v[32:35], v[120:123], v[36:39]
	v_mfma_f32_16x16x32_bf16 v[32:35], v[32:35], v[124:127], v[36:39]
	s_waitcnt lgkmcnt(0)
	v_mfma_f32_16x16x32_bf16 v[156:159], v[136:139], v[116:119], v[140:143]
	v_mfma_f32_16x16x32_bf16 v[32:35], v[136:139], v[128:131], v[32:35]
	ds_read_b128 v[136:139], v181 offset:53248
	s_nop 2
	ds_read_b128 v[140:143], v182 offset:53248
	s_waitcnt lgkmcnt(1)
	v_mfma_f32_16x16x32_bf16 v[164:167], v[136:139], v[120:123], v[36:39]
	v_mfma_f32_16x16x32_bf16 v[136:139], v[136:139], v[124:127], v[36:39]
	s_waitcnt lgkmcnt(0)
	v_mfma_f32_16x16x32_bf16 v[168:171], v[140:143], v[116:119], v[164:167]
	v_mfma_f32_16x16x32_bf16 v[140:143], v[140:143], v[128:131], v[136:139]
	s_nop 4
	ds_read_b128 v[136:139], v181 offset:57344
	ds_read_b128 v[184:187], v182 offset:57344
	s_waitcnt lgkmcnt(1)
	v_mfma_f32_16x16x32_bf16 v[164:167], v[136:139], v[120:123], v[36:39]
	v_mfma_f32_16x16x32_bf16 v[136:139], v[136:139], v[124:127], v[36:39]
	s_waitcnt lgkmcnt(0)
	v_mfma_f32_16x16x32_bf16 v[164:167], v[184:187], v[116:119], v[164:167]
	v_mfma_f32_16x16x32_bf16 v[136:139], v[184:187], v[128:131], v[136:139]
	ds_read_b128 v[184:187], v181 offset:61440
	ds_read_b128 v[188:191], v182 offset:61440
	s_waitcnt lgkmcnt(1)
	v_mfma_f32_16x16x32_bf16 v[120:123], v[184:187], v[120:123], v[36:39]
	s_waitcnt lgkmcnt(0)
	v_mfma_f32_16x16x32_bf16 v[116:119], v[188:191], v[116:119], v[120:123]
	v_mfma_f32_16x16x32_bf16 v[120:123], v[184:187], v[124:127], v[36:39]
	v_mfma_f32_16x16x32_bf16 v[128:131], v[188:191], v[128:131], v[120:123]
	s_nop 6
	v_add_u32_e32 v120, 0x10000, v180
	v_add_u32_e32 v181, v120, v178
	v_add_u32_e32 v190, v120, v179
	ds_read_b128 v[120:123], v181
	ds_read_b128 v[124:127], v190
	v_mfma_f32_16x16x128_f8f6f4 v[112:115], v[4:11], v[40:43], v[112:115] blgp:4
	v_mfma_f32_16x16x128_f8f6f4 v[88:91], v[12:19], v[40:43], v[88:91] blgp:4
	ds_read_b128 v[182:185], v181 offset:2048
	ds_read_b128 v[186:189], v190 offset:2048
	s_waitcnt lgkmcnt(2)
	v_mfma_f32_16x16x128_f8f6f4 v[108:111], v[4:11], v[120:127], v[108:111]
	v_mfma_f32_16x16x128_f8f6f4 v[80:83], v[12:19], v[120:127], v[80:83]
	ds_read_b128 v[120:123], v181 offset:4096
	ds_read_b128 v[124:127], v190 offset:4096
	s_waitcnt lgkmcnt(2)
	v_mfma_f32_16x16x128_f8f6f4 v[104:107], v[4:11], v[182:189], v[104:107]
	v_mfma_f32_16x16x128_f8f6f4 v[72:75], v[12:19], v[182:189], v[72:75]
	ds_read_b128 v[182:185], v181 offset:6144
	ds_read_b128 v[186:189], v190 offset:6144
	s_waitcnt lgkmcnt(2)
	v_mfma_f32_16x16x128_f8f6f4 v[100:103], v[4:11], v[120:127], v[100:103]
	v_mfma_f32_16x16x128_f8f6f4 v[64:67], v[12:19], v[120:127], v[64:67]
	ds_read_b128 v[120:123], v181 offset:8192
	ds_read_b128 v[124:127], v190 offset:8192
	s_waitcnt lgkmcnt(2)
	v_mfma_f32_16x16x128_f8f6f4 v[96:99], v[4:11], v[182:189], v[96:99]
	v_mfma_f32_16x16x128_f8f6f4 v[60:63], v[12:19], v[182:189], v[60:63]
	ds_read_b128 v[182:185], v181 offset:10240
	ds_read_b128 v[186:189], v190 offset:10240
	s_waitcnt lgkmcnt(2)
	v_mfma_f32_16x16x128_f8f6f4 v[92:95], v[4:11], v[120:127], v[92:95]
	v_mfma_f32_16x16x128_f8f6f4 v[56:59], v[12:19], v[120:127], v[56:59]
	ds_read_b128 v[120:123], v181 offset:12288
	ds_read_b128 v[124:127], v190 offset:12288
	s_waitcnt lgkmcnt(2)
	v_mfma_f32_16x16x128_f8f6f4 v[84:87], v[4:11], v[182:189], v[84:87]
	v_mfma_f32_16x16x128_f8f6f4 v[52:55], v[12:19], v[182:189], v[52:55]
	ds_read_b128 v[182:185], v181 offset:14336
	ds_read_b128 v[186:189], v190 offset:14336
	s_waitcnt lgkmcnt(2)
	v_mfma_f32_16x16x128_f8f6f4 v[76:79], v[4:11], v[120:127], v[76:79]
	v_mfma_f32_16x16x128_f8f6f4 v[48:51], v[12:19], v[120:127], v[48:51]
	s_waitcnt lgkmcnt(0)
	v_mfma_f32_16x16x128_f8f6f4 v[68:71], v[4:11], v[182:189], v[68:71]
	v_mfma_f32_16x16x128_f8f6f4 v[44:47], v[12:19], v[182:189], v[44:47]
	v_exp_f32_e32 v11, v128
	v_exp_f32_e32 v5, v129
	v_exp_f32_e32 v12, v144
	v_exp_f32_e32 v7, v145
	v_exp_f32_e32 v13, v152
	v_exp_f32_e32 v9, v153
	v_exp_f32_e32 v14, v148
	v_exp_f32_e32 v15, v149
	v_cvt_pk_fp8_f32 v11, v11, v5
	v_exp_f32_e32 v5, v146
	v_exp_f32_e32 v8, v147
	v_cvt_pk_fp8_f32 v12, v12, v7
	v_exp_f32_e32 v7, v154
	v_exp_f32_e32 v10, v155
	v_cvt_pk_fp8_f32 v13, v13, v9
	v_exp_f32_e32 v9, v150
	v_exp_f32_e32 v16, v151
	v_cvt_pk_fp8_f32 v14, v14, v15
	v_exp_f32_e32 v4, v130
	v_exp_f32_e32 v6, v131
	v_cvt_pk_fp8_f32 v12, v5, v8 op_sel:[0,0,1]
	v_cvt_pk_fp8_f32 v13, v7, v10 op_sel:[0,0,1]
	v_cvt_pk_fp8_f32 v14, v9, v16 op_sel:[0,0,1]
	v_exp_f32_e32 v15, v160
	v_exp_f32_e32 v5, v161
	v_exp_f32_e32 v16, v156
	v_exp_f32_e32 v7, v157
	v_cvt_pk_fp8_f32 v11, v4, v6 op_sel:[0,0,1]
	v_exp_f32_e32 v4, v162
	v_exp_f32_e32 v6, v163
	v_cvt_pk_fp8_f32 v15, v15, v5
	v_exp_f32_e32 v5, v158
	v_exp_f32_e32 v8, v159
	v_cvt_pk_fp8_f32 v16, v16, v7
	v_exp_f32_e32 v17, v168
	v_exp_f32_e32 v9, v169
	v_exp_f32_e32 v18, v164
	v_exp_f32_e32 v19, v165
	v_exp_f32_e32 v7, v170
	v_exp_f32_e32 v10, v171
	v_cvt_pk_fp8_f32 v17, v17, v9
	v_exp_f32_e32 v9, v166
	v_exp_f32_e32 v120, v167
	v_cvt_pk_fp8_f32 v18, v18, v19
	v_cvt_pk_fp8_f32 v15, v4, v6 op_sel:[0,0,1]
	v_cvt_pk_fp8_f32 v16, v5, v8 op_sel:[0,0,1]
	v_exp_f32_e32 v19, v116
	v_exp_f32_e32 v5, v117
	v_exp_f32_e32 v4, v20
	v_exp_f32_e32 v6, v21
	v_cvt_pk_fp8_f32 v17, v7, v10 op_sel:[0,0,1]
	v_cvt_pk_fp8_f32 v18, v9, v120 op_sel:[0,0,1]
	v_exp_f32_e32 v7, v118
	v_exp_f32_e32 v8, v119
	v_cvt_pk_fp8_f32 v19, v19, v5
	v_exp_f32_e32 v9, v22
	v_exp_f32_e32 v10, v23
	v_cvt_pk_fp8_f32 v4, v4, v6
	v_exp_f32_e32 v5, v28
	v_exp_f32_e32 v21, v29
	v_exp_f32_e32 v6, v24
	v_exp_f32_e32 v23, v25
	v_cvt_pk_fp8_f32 v19, v7, v8 op_sel:[0,0,1]
	v_cvt_pk_fp8_f32 v4, v9, v10 op_sel:[0,0,1]
	v_exp_f32_e32 v7, v132
	v_exp_f32_e32 v9, v133
	v_exp_f32_e32 v8, v32
	v_exp_f32_e32 v10, v33
	v_exp_f32_e32 v20, v30
	v_exp_f32_e32 v22, v31
	v_cvt_pk_fp8_f32 v5, v5, v21
	v_exp_f32_e32 v21, v26
	v_exp_f32_e32 v24, v27
	v_cvt_pk_fp8_f32 v6, v6, v23
	v_cvt_pk_fp8_f32 v7, v7, v9
	v_cvt_pk_fp8_f32 v8, v8, v10
	v_exp_f32_e32 v9, v140
	v_exp_f32_e32 v25, v141
	v_exp_f32_e32 v10, v136
	v_exp_f32_e32 v27, v137
	v_cvt_pk_fp8_f32 v5, v20, v22 op_sel:[0,0,1]
	v_cvt_pk_fp8_f32 v6, v21, v24 op_sel:[0,0,1]
	v_exp_f32_e32 v20, v134
	v_exp_f32_e32 v21, v135
	v_cvt_pk_fp8_f32 v9, v9, v25
	v_exp_f32_e32 v25, v138
	v_exp_f32_e32 v28, v139
	v_cvt_pk_fp8_f32 v10, v10, v27
	v_exp_f32_e32 v22, v34
	v_exp_f32_e32 v23, v35
	v_exp_f32_e32 v24, v142
	v_exp_f32_e32 v26, v143
	v_cvt_pk_fp8_f32 v7, v20, v21 op_sel:[0,0,1]
	v_add_u32_e32 v20, 0x14000, v180
	v_cvt_pk_fp8_f32 v10, v25, v28 op_sel:[0,0,1]
	v_add_u32_e32 v28, v20, v178
	v_cvt_pk_fp8_f32 v8, v22, v23 op_sel:[0,0,1]
	v_cvt_pk_fp8_f32 v9, v24, v26 op_sel:[0,0,1]
	s_nop 1
	v_mfma_f32_16x16x128_f8f6f4 v[112:115], v[12:19], v[40:43], v[112:115] blgp:4
	v_add_u32_e32 v29, v20, v179
	v_mfma_f32_16x16x128_f8f6f4 v[88:91], v[4:11], v[40:43], v[88:91] blgp:4
	ds_read_b128 v[20:23], v28
	ds_read_b128 v[24:27], v29
	s_waitcnt lgkmcnt(0)
	v_mfma_f32_16x16x128_f8f6f4 v[108:111], v[12:19], v[20:27], v[108:111]
	v_mfma_f32_16x16x128_f8f6f4 v[80:83], v[4:11], v[20:27], v[80:83]
	ds_read_b128 v[20:23], v28 offset:2048
	ds_read_b128 v[24:27], v29 offset:2048
	s_waitcnt lgkmcnt(0)
	v_mfma_f32_16x16x128_f8f6f4 v[104:107], v[12:19], v[20:27], v[104:107]
	v_mfma_f32_16x16x128_f8f6f4 v[72:75], v[4:11], v[20:27], v[72:75]
	ds_read_b128 v[20:23], v28 offset:4096
	ds_read_b128 v[24:27], v29 offset:4096
	s_waitcnt lgkmcnt(0)
	v_mfma_f32_16x16x128_f8f6f4 v[100:103], v[12:19], v[20:27], v[100:103]
	v_mfma_f32_16x16x128_f8f6f4 v[64:67], v[4:11], v[20:27], v[64:67]
	ds_read_b128 v[20:23], v28 offset:6144
	ds_read_b128 v[24:27], v29 offset:6144
	s_waitcnt lgkmcnt(0)
	v_mfma_f32_16x16x128_f8f6f4 v[96:99], v[12:19], v[20:27], v[96:99]
	v_mfma_f32_16x16x128_f8f6f4 v[60:63], v[4:11], v[20:27], v[60:63]
	ds_read_b128 v[20:23], v28 offset:8192
	ds_read_b128 v[24:27], v29 offset:8192
	s_waitcnt lgkmcnt(0)
	v_mfma_f32_16x16x128_f8f6f4 v[92:95], v[12:19], v[20:27], v[92:95]
	v_mfma_f32_16x16x128_f8f6f4 v[56:59], v[4:11], v[20:27], v[56:59]
	ds_read_b128 v[20:23], v28 offset:10240
	ds_read_b128 v[24:27], v29 offset:10240
	s_waitcnt lgkmcnt(0)
	v_mfma_f32_16x16x128_f8f6f4 v[84:87], v[12:19], v[20:27], v[84:87]
	v_mfma_f32_16x16x128_f8f6f4 v[52:55], v[4:11], v[20:27], v[52:55]
	ds_read_b128 v[20:23], v28 offset:12288
	ds_read_b128 v[24:27], v29 offset:12288
	s_waitcnt lgkmcnt(0)
	v_mfma_f32_16x16x128_f8f6f4 v[76:79], v[12:19], v[20:27], v[76:79]
	v_mfma_f32_16x16x128_f8f6f4 v[48:51], v[4:11], v[20:27], v[48:51]
	ds_read_b128 v[20:23], v28 offset:14336
	ds_read_b128 v[24:27], v29 offset:14336
	s_waitcnt lgkmcnt(0)
	v_mfma_f32_16x16x128_f8f6f4 v[68:71], v[12:19], v[20:27], v[68:71]
	v_mfma_f32_16x16x128_f8f6f4 v[44:47], v[4:11], v[20:27], v[44:47]
	v_rcp_f32_e32 v4, v112
	v_rcp_f32_e32 v6, v113
	s_nop 15
	s_nop 15
	v_readlane_b32 s4, v253, 16
	v_mul_f32_e32 v8, v4, v108
	v_mul_f32_e32 v10, v4, v104
	v_mul_f32_e32 v12, v4, v100
	v_mul_f32_e32 v14, v4, v96
	v_mul_f32_e32 v16, v4, v92
	v_mul_f32_e32 v18, v4, v84
	v_mul_f32_e32 v20, v4, v76
	v_mul_f32_e32 v5, v4, v68
	v_mul_f32_e32 v118, v6, v109
	v_mul_f32_e32 v119, v6, v105
	v_mul_f32_e32 v117, v6, v101
	v_mul_f32_e32 v116, v6, v97
	v_mul_f32_e32 v112, v6, v93
	v_rcp_f32_e32 v4, v114
	v_mul_f32_e32 v114, v6, v85
	v_mul_f32_e32 v113, v6, v77
	v_mul_f32_e32 v109, v6, v69
	v_rcp_f32_e32 v6, v115
	v_mul_f32_e32 v108, v4, v110
	v_mul_f32_e32 v105, v4, v106
	v_mul_f32_e32 v104, v4, v102
	v_mul_f32_e32 v102, v4, v98
	v_mul_f32_e32 v101, v4, v94
	v_mul_f32_e32 v100, v4, v86
	v_mul_f32_e32 v98, v4, v78
	v_mul_f32_e32 v97, v4, v70
	v_mul_f32_e32 v94, v6, v111
	v_mul_f32_e32 v96, v6, v107
	v_mul_f32_e32 v93, v6, v103
	v_mul_f32_e32 v92, v6, v99
	v_mul_f32_e32 v86, v6, v95
	v_rcp_f32_e32 v4, v88
	v_mul_f32_e32 v88, v6, v87
	v_mul_f32_e32 v87, v6, v79
	v_mul_f32_e32 v85, v6, v71
	v_rcp_f32_e32 v6, v89
	v_mul_f32_e32 v84, v4, v80
	v_mul_f32_e32 v80, v4, v72
	v_mul_f32_e32 v79, v4, v64
	v_mul_f32_e32 v78, v4, v60
	v_mul_f32_e32 v77, v4, v56
	v_mul_f32_e32 v23, v4, v52
	v_mul_f32_e32 v22, v4, v48
	v_mul_f32_e32 v76, v4, v44
	v_mul_f32_e32 v72, v6, v81
	v_mul_f32_e32 v73, v6, v73
	v_mul_f32_e32 v71, v6, v65
	v_mul_f32_e32 v69, v6, v61
	v_mul_f32_e32 v65, v6, v57
	v_rcp_f32_e32 v4, v90
	v_mul_f32_e32 v70, v6, v53
	v_mul_f32_e32 v68, v6, v49
	v_mul_f32_e32 v64, v6, v45
	v_rcp_f32_e32 v6, v91
	v_readlane_b32 s5, v253, 17
	v_mul_f32_e32 v61, v4, v82
	v_mul_f32_e32 v60, v4, v74
	v_mul_f32_e32 v57, v4, v66
	v_mul_f32_e32 v56, v4, v62
	v_mul_f32_e32 v53, v4, v58
	v_mul_f32_e32 v52, v4, v54
	v_mul_f32_e32 v49, v4, v50
	v_mul_f32_e32 v48, v4, v46
	v_mul_f32_e32 v42, v6, v83
	v_mul_f32_e32 v43, v6, v75
	v_mul_f32_e32 v41, v6, v67
	v_mul_f32_e32 v40, v6, v63
	v_mul_f32_e32 v34, v6, v59
	v_mul_f32_e32 v33, v6, v55
	v_mul_f32_e32 v32, v6, v51
	s_andn2_b64 vcc, exec, s[4:5]
	v_mul_f32_e32 v35, v6, v47
	s_waitcnt vmcnt(0)
	s_barrier
	s_cbranch_vccnz .LBB0_377
	v_add_u32_e32 v4, s84, v2
	v_lshl_add_u32 v4, v4, 2, 0
	ds_write2st64_b32 v4, v8, v118 offset1:4
	ds_write2st64_b32 v4, v108, v94 offset0:8 offset1:12
	ds_write2st64_b32 v4, v10, v119 offset0:16 offset1:20
	ds_write2st64_b32 v4, v105, v96 offset0:24 offset1:28
	ds_write2st64_b32 v4, v12, v117 offset0:32 offset1:36
	ds_write2st64_b32 v4, v104, v93 offset0:40 offset1:44
	ds_write2st64_b32 v4, v14, v116 offset0:48 offset1:52
	ds_write2st64_b32 v4, v102, v92 offset0:56 offset1:60
	ds_write2st64_b32 v4, v16, v112 offset0:64 offset1:68
	ds_write2st64_b32 v4, v101, v86 offset0:72 offset1:76
	ds_write2st64_b32 v4, v18, v114 offset0:80 offset1:84
	ds_write2st64_b32 v4, v100, v88 offset0:88 offset1:92
	ds_write2st64_b32 v4, v20, v113 offset0:96 offset1:100
	ds_write2st64_b32 v4, v98, v87 offset0:104 offset1:108
	ds_write2st64_b32 v4, v5, v109 offset0:112 offset1:116
	ds_write2st64_b32 v4, v97, v85 offset0:120 offset1:124
	ds_write2st64_b32 v4, v84, v72 offset0:128 offset1:132
	ds_write2st64_b32 v4, v61, v42 offset0:136 offset1:140
	ds_write2st64_b32 v4, v80, v73 offset0:144 offset1:148
	ds_write2st64_b32 v4, v60, v43 offset0:152 offset1:156
	ds_write2st64_b32 v4, v79, v71 offset0:160 offset1:164
	ds_write2st64_b32 v4, v57, v41 offset0:168 offset1:172
	ds_write2st64_b32 v4, v78, v69 offset0:176 offset1:180
	ds_write2st64_b32 v4, v56, v40 offset0:184 offset1:188
	ds_write2st64_b32 v4, v77, v65 offset0:192 offset1:196
	ds_write2st64_b32 v4, v53, v34 offset0:200 offset1:204
	ds_write2st64_b32 v4, v23, v70 offset0:208 offset1:212
	ds_write2st64_b32 v4, v52, v33 offset0:216 offset1:220
	ds_write2st64_b32 v4, v22, v68 offset0:224 offset1:228
	ds_write2st64_b32 v4, v49, v32 offset0:232 offset1:236
	ds_write2st64_b32 v4, v76, v64 offset0:240 offset1:244
	ds_write2st64_b32 v4, v48, v35 offset0:248 offset1:252

.LBB0_882:
	s_ashr_i32 s5, s4, 31
	s_lshl_b64 s[12:13], s[4:5], 2
	s_add_u32 s14, s0, s12
	s_addc_u32 s15, s3, s13
	global_load_dwordx2 v[12:13], v3, s[14:15]
	s_add_i32 s14, s4, 1
	s_ashr_i32 s15, s14, 31
	s_add_u32 s12, s6, s12
	s_addc_u32 s13, s7, s13
	global_load_dword v8, v3, s[12:13]
	s_lshl_b64 s[12:13], s[14:15], 2
	s_add_u32 s12, s6, s12
	s_addc_u32 s13, s7, s13
	global_load_dword v10, v3, s[12:13]
	s_add_i32 s8, s8, s52
	s_add_i32 s4, s4, s29
	s_cmpk_lt_i32 s8, 0x4000
	s_waitcnt vmcnt(2)
	v_pk_mul_f32 v[12:13], v[12:13], s[82:83] op_sel:[1,0] op_sel_hi:[0,0]
	s_waitcnt vmcnt(1)
	v_ashrrev_i32_e32 v9, 31, v8
	v_lshlrev_b64 v[8:9], 12, v[8:9]
	v_lshl_add_u64 v[8:9], v[0:1], 0, v[8:9]
	s_waitcnt vmcnt(0)
	v_ashrrev_i32_e32 v11, 31, v10
	v_lshlrev_b64 v[10:11], 12, v[10:11]
	v_lshl_add_u64 v[10:11], v[0:1], 0, v[10:11]
	global_load_dwordx2 v[16:17], v[6:7], off offset:-2048 nt
	global_load_dwordx2 v[18:19], v[8:9], off nt
	global_load_dwordx2 v[20:21], v[10:11], off nt
	s_waitcnt vmcnt(2)
	v_lshlrev_b32_e32 v14, 16, v16
	s_waitcnt vmcnt(1)
	v_lshlrev_b32_e32 v24, 16, v18
	s_waitcnt vmcnt(0)
	v_and_b32_e32 v25, 0xffff0000, v20
	v_lshlrev_b32_e32 v22, 16, v20
	v_and_b32_e32 v23, 0xffff0000, v18
	v_pk_mul_f32 v[24:25], v[12:13], v[24:25] op_sel:[1,0] op_sel_hi:[0,1]
	v_and_b32_e32 v15, 0xffff0000, v16
	v_pk_fma_f32 v[22:23], v[12:13], v[22:23], v[24:25]
	v_lshlrev_b32_e32 v18, 16, v19
	v_pk_add_f32 v[14:15], v[22:23], v[14:15]
	v_and_b32_e32 v23, 0xffff0000, v19
	v_and_b32_e32 v19, 0xffff0000, v21
	v_lshlrev_b32_e32 v22, 16, v21
	v_pk_mul_f32 v[18:19], v[12:13], v[18:19] op_sel:[1,0] op_sel_hi:[0,1]
	v_lshlrev_b32_e32 v16, 16, v17
	v_and_b32_e32 v17, 0xffff0000, v17
	v_pk_fma_f32 v[18:19], v[12:13], v[22:23], v[18:19]
	s_nop 0
	v_pk_add_f32 v[16:17], v[18:19], v[16:17]
	global_store_dwordx4 v[4:5], v[14:17], off offset:-4096
	global_load_dwordx2 v[16:17], v[6:7], off offset:-1536 nt
	s_nop 0
	global_load_dwordx2 v[18:19], v[8:9], off offset:512 nt
	global_load_dwordx2 v[20:21], v[10:11], off offset:512 nt
	s_waitcnt vmcnt(2)
	v_lshlrev_b32_e32 v14, 16, v16
	s_waitcnt vmcnt(1)
	v_lshlrev_b32_e32 v24, 16, v18
	s_waitcnt vmcnt(0)
	v_and_b32_e32 v25, 0xffff0000, v20
	v_lshlrev_b32_e32 v22, 16, v20
	v_and_b32_e32 v23, 0xffff0000, v18
	v_pk_mul_f32 v[24:25], v[12:13], v[24:25] op_sel:[1,0] op_sel_hi:[0,1]
	v_and_b32_e32 v15, 0xffff0000, v16
	v_pk_fma_f32 v[22:23], v[12:13], v[22:23], v[24:25]
	v_lshlrev_b32_e32 v18, 16, v19
	v_pk_add_f32 v[14:15], v[22:23], v[14:15]
	v_and_b32_e32 v23, 0xffff0000, v19
	v_and_b32_e32 v19, 0xffff0000, v21
	v_lshlrev_b32_e32 v22, 16, v21
	v_pk_mul_f32 v[18:19], v[12:13], v[18:19] op_sel:[1,0] op_sel_hi:[0,1]
	v_lshlrev_b32_e32 v16, 16, v17
	v_and_b32_e32 v17, 0xffff0000, v17
	v_pk_fma_f32 v[18:19], v[12:13], v[22:23], v[18:19]
	s_nop 0
	v_pk_add_f32 v[16:17], v[18:19], v[16:17]
	global_store_dwordx4 v[4:5], v[14:17], off offset:-3072
	global_load_dwordx2 v[16:17], v[6:7], off offset:-1024 nt
	s_nop 0
	global_load_dwordx2 v[18:19], v[8:9], off offset:1024 nt
	global_load_dwordx2 v[20:21], v[10:11], off offset:1024 nt
	s_waitcnt vmcnt(2)
	v_lshlrev_b32_e32 v14, 16, v16
	s_waitcnt vmcnt(1)
	v_lshlrev_b32_e32 v24, 16, v18
	s_waitcnt vmcnt(0)
	v_and_b32_e32 v25, 0xffff0000, v20
	v_lshlrev_b32_e32 v22, 16, v20
	v_and_b32_e32 v23, 0xffff0000, v18
	v_pk_mul_f32 v[24:25], v[12:13], v[24:25] op_sel:[1,0] op_sel_hi:[0,1]
	v_and_b32_e32 v15, 0xffff0000, v16
	v_pk_fma_f32 v[22:23], v[12:13], v[22:23], v[24:25]
	v_lshlrev_b32_e32 v18, 16, v19
	v_pk_add_f32 v[14:15], v[22:23], v[14:15]
	v_and_b32_e32 v23, 0xffff0000, v19
	v_and_b32_e32 v19, 0xffff0000, v21
	v_lshlrev_b32_e32 v22, 16, v21
	v_pk_mul_f32 v[18:19], v[12:13], v[18:19] op_sel:[1,0] op_sel_hi:[0,1]
	v_lshlrev_b32_e32 v16, 16, v17
	v_and_b32_e32 v17, 0xffff0000, v17
	v_pk_fma_f32 v[18:19], v[12:13], v[22:23], v[18:19]
	s_nop 0
	v_pk_add_f32 v[16:17], v[18:19], v[16:17]
	global_store_dwordx4 v[4:5], v[14:17], off offset:-2048
	global_load_dwordx2 v[16:17], v[6:7], off offset:-512 nt
	s_nop 0
	global_load_dwordx2 v[18:19], v[8:9], off offset:1536 nt
	global_load_dwordx2 v[20:21], v[10:11], off offset:1536 nt
	s_waitcnt vmcnt(2)
	v_lshlrev_b32_e32 v14, 16, v16
	s_waitcnt vmcnt(1)
	v_lshlrev_b32_e32 v24, 16, v18
	s_waitcnt vmcnt(0)
	v_and_b32_e32 v25, 0xffff0000, v20
	v_lshlrev_b32_e32 v22, 16, v20
	v_and_b32_e32 v23, 0xffff0000, v18
	v_pk_mul_f32 v[24:25], v[12:13], v[24:25] op_sel:[1,0] op_sel_hi:[0,1]
	v_and_b32_e32 v15, 0xffff0000, v16
	v_pk_fma_f32 v[22:23], v[12:13], v[22:23], v[24:25]
	v_lshlrev_b32_e32 v18, 16, v19
	v_pk_add_f32 v[14:15], v[22:23], v[14:15]
	v_and_b32_e32 v23, 0xffff0000, v19
	v_and_b32_e32 v19, 0xffff0000, v21
	v_lshlrev_b32_e32 v22, 16, v21
	v_pk_mul_f32 v[18:19], v[12:13], v[18:19] op_sel:[1,0] op_sel_hi:[0,1]
	v_lshlrev_b32_e32 v16, 16, v17
	v_and_b32_e32 v17, 0xffff0000, v17
	v_pk_fma_f32 v[18:19], v[12:13], v[22:23], v[18:19]
	s_nop 0
	v_pk_add_f32 v[16:17], v[18:19], v[16:17]
	global_store_dwordx4 v[4:5], v[14:17], off offset:-1024
	global_load_dwordx2 v[16:17], v[6:7], off nt
	s_nop 0
	global_load_dwordx2 v[18:19], v[8:9], off offset:2048 nt
	global_load_dwordx2 v[20:21], v[10:11], off offset:2048 nt
	s_waitcnt vmcnt(2)
	v_lshlrev_b32_e32 v14, 16, v16
	s_waitcnt vmcnt(1)
	v_lshlrev_b32_e32 v24, 16, v18
	s_waitcnt vmcnt(0)
	v_and_b32_e32 v25, 0xffff0000, v20
	v_lshlrev_b32_e32 v22, 16, v20
	v_and_b32_e32 v23, 0xffff0000, v18
	v_pk_mul_f32 v[24:25], v[12:13], v[24:25] op_sel:[1,0] op_sel_hi:[0,1]
	v_and_b32_e32 v15, 0xffff0000, v16
	v_pk_fma_f32 v[22:23], v[12:13], v[22:23], v[24:25]
	v_lshlrev_b32_e32 v18, 16, v19
	v_pk_add_f32 v[14:15], v[22:23], v[14:15]
	v_and_b32_e32 v23, 0xffff0000, v19
	v_and_b32_e32 v19, 0xffff0000, v21
	v_lshlrev_b32_e32 v22, 16, v21
	v_pk_mul_f32 v[18:19], v[12:13], v[18:19] op_sel:[1,0] op_sel_hi:[0,1]
	v_lshlrev_b32_e32 v16, 16, v17
	v_and_b32_e32 v17, 0xffff0000, v17
	v_pk_fma_f32 v[18:19], v[12:13], v[22:23], v[18:19]
	s_nop 0
	v_pk_add_f32 v[16:17], v[18:19], v[16:17]
	global_store_dwordx4 v[4:5], v[14:17], off
	global_load_dwordx2 v[16:17], v[6:7], off offset:512 nt
	s_nop 0
	global_load_dwordx2 v[18:19], v[8:9], off offset:2560 nt
	global_load_dwordx2 v[20:21], v[10:11], off offset:2560 nt
	s_waitcnt vmcnt(2)
	v_lshlrev_b32_e32 v14, 16, v16
	s_waitcnt vmcnt(1)
	v_lshlrev_b32_e32 v24, 16, v18
	s_waitcnt vmcnt(0)
	v_and_b32_e32 v25, 0xffff0000, v20
	v_lshlrev_b32_e32 v22, 16, v20
	v_and_b32_e32 v23, 0xffff0000, v18
	v_pk_mul_f32 v[24:25], v[12:13], v[24:25] op_sel:[1,0] op_sel_hi:[0,1]
	v_and_b32_e32 v15, 0xffff0000, v16
	v_pk_fma_f32 v[22:23], v[12:13], v[22:23], v[24:25]
	v_lshlrev_b32_e32 v18, 16, v19
	v_pk_add_f32 v[14:15], v[22:23], v[14:15]
	v_and_b32_e32 v23, 0xffff0000, v19
	v_and_b32_e32 v19, 0xffff0000, v21
	v_lshlrev_b32_e32 v22, 16, v21
	v_pk_mul_f32 v[18:19], v[12:13], v[18:19] op_sel:[1,0] op_sel_hi:[0,1]
	v_lshlrev_b32_e32 v16, 16, v17
	v_and_b32_e32 v17, 0xffff0000, v17
	v_pk_fma_f32 v[18:19], v[12:13], v[22:23], v[18:19]
	s_nop 0
	v_pk_add_f32 v[16:17], v[18:19], v[16:17]
	global_store_dwordx4 v[4:5], v[14:17], off offset:1024
	global_load_dwordx2 v[16:17], v[6:7], off offset:1024 nt
	s_nop 0
	global_load_dwordx2 v[18:19], v[8:9], off offset:3072 nt
	global_load_dwordx2 v[20:21], v[10:11], off offset:3072 nt
	s_waitcnt vmcnt(2)
	v_lshlrev_b32_e32 v14, 16, v16
	s_waitcnt vmcnt(1)
	v_lshlrev_b32_e32 v24, 16, v18
	s_waitcnt vmcnt(0)
	v_and_b32_e32 v25, 0xffff0000, v20
	v_lshlrev_b32_e32 v22, 16, v20
	v_and_b32_e32 v23, 0xffff0000, v18
	v_pk_mul_f32 v[24:25], v[12:13], v[24:25] op_sel:[1,0] op_sel_hi:[0,1]
	v_and_b32_e32 v15, 0xffff0000, v16
	v_pk_fma_f32 v[22:23], v[12:13], v[22:23], v[24:25]
	v_lshlrev_b32_e32 v18, 16, v19
	v_pk_add_f32 v[14:15], v[22:23], v[14:15]
	v_and_b32_e32 v23, 0xffff0000, v19
	v_and_b32_e32 v19, 0xffff0000, v21
	v_lshlrev_b32_e32 v22, 16, v21
	v_pk_mul_f32 v[18:19], v[12:13], v[18:19] op_sel:[1,0] op_sel_hi:[0,1]
	v_lshlrev_b32_e32 v16, 16, v17
	v_and_b32_e32 v17, 0xffff0000, v17
	v_pk_fma_f32 v[18:19], v[12:13], v[22:23], v[18:19]
	s_nop 0
	v_pk_add_f32 v[16:17], v[18:19], v[16:17]
	global_store_dwordx4 v[4:5], v[14:17], off offset:2048
	global_load_dwordx2 v[14:15], v[6:7], off offset:1536 nt
	s_nop 0
	global_load_dwordx2 v[16:17], v[8:9], off offset:3584 nt
	s_nop 0
	global_load_dwordx2 v[10:11], v[10:11], off offset:3584 nt
	v_lshl_add_u64 v[6:7], v[6:7], 0, s[78:79]
	s_waitcnt vmcnt(2)
	v_lshlrev_b32_e32 v8, 16, v14
	s_waitcnt vmcnt(1)
	v_lshlrev_b32_e32 v20, 16, v16
	s_waitcnt vmcnt(0)
	v_and_b32_e32 v21, 0xffff0000, v10
	v_lshlrev_b32_e32 v18, 16, v10
	v_and_b32_e32 v19, 0xffff0000, v16
	v_pk_mul_f32 v[20:21], v[12:13], v[20:21] op_sel:[1,0] op_sel_hi:[0,1]
	v_and_b32_e32 v9, 0xffff0000, v14
	v_pk_fma_f32 v[18:19], v[12:13], v[18:19], v[20:21]
	v_lshlrev_b32_e32 v10, 16, v17
	v_pk_add_f32 v[8:9], v[18:19], v[8:9]
	v_lshlrev_b32_e32 v18, 16, v11
	v_and_b32_e32 v11, 0xffff0000, v11
	v_and_b32_e32 v19, 0xffff0000, v17
	v_pk_mul_f32 v[10:11], v[12:13], v[10:11] op_sel:[1,0] op_sel_hi:[0,1]
	v_lshlrev_b32_e32 v14, 16, v15
	v_and_b32_e32 v15, 0xffff0000, v15
	v_pk_fma_f32 v[10:11], v[12:13], v[18:19], v[10:11]
	s_nop 0
	v_pk_add_f32 v[10:11], v[10:11], v[14:15]
	global_store_dwordx4 v[4:5], v[8:11], off offset:3072
	v_lshl_add_u64 v[4:5], v[4:5], 0, s[50:51]
	s_cbranch_scc1 .LBB0_882
